# stack4 = stack3 + batched loads in the ada final sum and in the NAT bias-table fill
# speedup vs baseline: 1.0034x; 1.0034x over previous
.LBB0_24:
	s_mov_b32 s0, 0xcccccccd
	v_mul_hi_u32 v5, v4, s0
	s_mov_b32 s0, 0xcccd
	v_mul_u32_u24_sdwa v6, v4, s0 dst_sel:DWORD dst_unused:UNUSED_PAD src0_sel:WORD_0 src1_sel:DWORD
	v_lshl_add_u64 v[14:15], s[14:15], 0, v[162:163]
	v_lshrrev_b32_e32 v16, 24, v6
	v_lshrrev_b32_e32 v5, 8, v5
	v_add_co_u32_e32 v128, vcc, 0x1cb00000, v14
	s_nop 1
	v_addc_co_u32_e32 v129, vcc, 0, v15, vcc
	global_load_dwordx4 v[6:9], v[128:129], off
	v_add_co_u32_e32 v128, vcc, 0x1cb03000, v14
	s_nop 1
	v_addc_co_u32_e32 v129, vcc, 0, v15, vcc
	global_load_dwordx4 v[10:13], v[128:129], off offset:3072
	v_add_co_u32_e32 v128, vcc, 0x1cb07000, v14
	s_nop 1
	v_addc_co_u32_e32 v129, vcc, 0, v15, vcc
	global_load_dwordx4 v[18:21], v[128:129], off offset:2048
	v_add_co_u32_e32 v128, vcc, 0x1cb0b000, v14
	s_nop 1
	v_addc_co_u32_e32 v129, vcc, 0, v15, vcc
	global_load_dwordx4 v[22:25], v[128:129], off offset:1024
	v_add_co_u32_e32 v128, vcc, 0x1cb0f000, v14
	s_nop 1
	v_addc_co_u32_e32 v129, vcc, 0, v15, vcc
	global_load_dwordx4 v[26:29], v[128:129], off
	v_add_co_u32_e32 v128, vcc, 0x1cb12000, v14
	s_nop 1
	v_addc_co_u32_e32 v129, vcc, 0, v15, vcc
	global_load_dwordx4 v[30:33], v[128:129], off offset:3072
	v_add_co_u32_e32 v128, vcc, 0x1cb16000, v14
	s_nop 1
	v_addc_co_u32_e32 v129, vcc, 0, v15, vcc
	global_load_dwordx4 v[34:37], v[128:129], off offset:2048
	v_lshl_add_u64 v[128:129], s[18:19], 0, v[162:163]
	global_load_dwordx4 v[120:123], v[128:129], off
	v_lshl_add_u32 v128, v16, 8, s34
	v_and_or_b32 v128, v3, s31, v128
	v_lshlrev_b32_e32 v158, 2, v128
	global_load_dwordx4 v[124:127], v158, s[16:17]
	s_add_u32 s14, s14, 0x2000
	v_mul_u32_u24_e32 v5, 5, v5
	s_addc_u32 s15, s15, 0
	v_sub_u32_e32 v5, v2, v5
	v_add_u32_e32 v2, 8, v2
	s_add_u32 s18, s18, 0x2000
	s_addc_u32 s19, s19, 0
	v_add_u32_e32 v3, 0x800, v3
	v_cmp_lt_u32_e32 vcc, s30, v4
	s_waitcnt vmcnt(7)
	v_pk_add_f32 v[10:11], v[6:7], v[10:11]
	v_pk_add_f32 v[12:13], v[8:9], v[12:13]
	s_waitcnt vmcnt(6)
	v_pk_add_f32 v[10:11], v[10:11], v[18:19]
	v_pk_add_f32 v[12:13], v[12:13], v[20:21]
	s_waitcnt vmcnt(5)
	v_pk_add_f32 v[10:11], v[10:11], v[22:23]
	v_pk_add_f32 v[12:13], v[12:13], v[24:25]
	s_waitcnt vmcnt(4)
	v_pk_add_f32 v[10:11], v[10:11], v[26:27]
	v_pk_add_f32 v[12:13], v[12:13], v[28:29]
	s_waitcnt vmcnt(3)
	v_pk_add_f32 v[10:11], v[10:11], v[30:31]
	v_pk_add_f32 v[12:13], v[12:13], v[32:33]
	s_waitcnt vmcnt(2)
	v_pk_add_f32 v[10:11], v[10:11], v[34:35]
	v_pk_add_f32 v[12:13], v[12:13], v[36:37]
	s_waitcnt vmcnt(1)
	v_pk_add_f32 v[10:11], v[10:11], v[120:121]
	v_pk_add_f32 v[12:13], v[12:13], v[122:123]
	s_or_b64 s[20:21], vcc, s[20:21]
	s_waitcnt vmcnt(0)
	v_pk_add_f32 v[6:7], v[10:11], v[124:125]
	v_mov_b64_e32 v[10:11], s[6:7]
	v_mad_i64_i32 v[10:11], s[36:37], v5, s29, v[10:11]
	v_add_u32_e32 v5, 0x200, v4
	v_pk_add_f32 v[8:9], v[12:13], v[126:127]
	v_lshl_add_u64 v[10:11], v[10:11], 0, v[158:159]
	v_mov_b32_e32 v4, v5
	global_store_dwordx4 v[10:11], v[6:9], off
	s_andn2_b64 exec, exec, s[20:21]
	s_cbranch_execnz .LBB0_24
	s_branch .LBB0_8

.LBB0_1573:
	s_cmp_lt_i32 s86, 13
	s_cselect_b64 s[0:1], -1, 0
	s_and_b64 s[4:5], s[0:1], s[4:5]
	s_andn2_b64 vcc, exec, s[4:5]
	s_cbranch_vccnz .LBB0_1684
	s_abs_i32 s2, s94
	s_waitcnt vmcnt(0)
	v_cvt_f32_u32_e32 v2, s2
	s_sub_i32 s0, s94, s90
	s_add_i32 s1, s0, 0x3ff
	s_sub_i32 s0, 0xfffffc01, s0
	v_rcp_iflag_f32_e32 v2, v2
	s_sub_i32 s6, 0, s2
	s_max_i32 s11, s1, s0
	v_lshrrev_b32_e32 v26, 5, v0
	v_mul_f32_e32 v2, 0x4f7ffffe, v2
	v_cvt_u32_f32_e32 v2, v2
	v_and_b32_e32 v3, 31, v0
	s_ashr_i32 s12, s1, 31
	v_cmp_ne_u32_e32 vcc, 31, v3
	v_readfirstlane_b32 s0, v2
	s_mul_i32 s6, s6, s0
	s_mul_hi_u32 s1, s0, s6
	v_mul_u32_u24_e32 v2, 31, v26
	s_add_i32 s0, s0, s1
	v_add_lshl_u32 v2, v2, v3, 2
	v_mov_b32_e32 v3, 0
	s_ashr_i32 s10, s94, 31
	s_mul_hi_u32 s13, s11, s0
	v_add_u32_e32 v4, 0xa800, v254
	v_lshl_add_u64 v[2:3], s[48:49], 0, v[2:3]
	v_or_b32_e32 v5, 0xfffffe00, v0
	s_mov_b64 s[6:7], 0
	s_mov_b64 s[8:9], 0x7c0
	s_movk_i32 s14, 0x1bff
	s_mov_b64 s[0:1], exec
	v_mov_b32_e32 v7, 0xff800000
	v_mov_b32_e32 v8, 0xff800000
	v_mov_b32_e32 v9, 0xff800000
	v_mov_b32_e32 v10, 0xff800000
	v_mov_b32_e32 v11, 0xff800000
	v_mov_b32_e32 v12, 0xff800000
	v_mov_b32_e32 v13, 0xff800000
	v_mov_b32_e32 v14, 0xff800000
	v_mov_b32_e32 v15, 0xff800000
	v_mov_b32_e32 v16, 0xff800000
	v_mov_b32_e32 v17, 0xff800000
	v_mov_b32_e32 v18, 0xff800000
	v_mov_b32_e32 v19, 0xff800000
	v_mov_b32_e32 v20, 0xff800000
	v_mov_b32_e32 v21, 0xff800000
	s_and_b64 exec, s[0:1], vcc
	global_load_dword v7, v[2:3], off
	v_lshl_add_u64 v[2:3], v[2:3], 0, s[8:9]
	global_load_dword v8, v[2:3], off
	v_lshl_add_u64 v[2:3], v[2:3], 0, s[8:9]
	global_load_dword v9, v[2:3], off
	v_lshl_add_u64 v[2:3], v[2:3], 0, s[8:9]
	global_load_dword v10, v[2:3], off
	v_lshl_add_u64 v[2:3], v[2:3], 0, s[8:9]
	global_load_dword v11, v[2:3], off
	v_lshl_add_u64 v[2:3], v[2:3], 0, s[8:9]
	global_load_dword v12, v[2:3], off
	v_lshl_add_u64 v[2:3], v[2:3], 0, s[8:9]
	global_load_dword v13, v[2:3], off
	v_lshl_add_u64 v[2:3], v[2:3], 0, s[8:9]
	global_load_dword v14, v[2:3], off
	v_lshl_add_u64 v[2:3], v[2:3], 0, s[8:9]
	global_load_dword v15, v[2:3], off
	v_lshl_add_u64 v[2:3], v[2:3], 0, s[8:9]
	global_load_dword v16, v[2:3], off
	v_lshl_add_u64 v[2:3], v[2:3], 0, s[8:9]
	global_load_dword v17, v[2:3], off
	v_lshl_add_u64 v[2:3], v[2:3], 0, s[8:9]
	global_load_dword v18, v[2:3], off
	v_lshl_add_u64 v[2:3], v[2:3], 0, s[8:9]
	global_load_dword v19, v[2:3], off
	v_lshl_add_u64 v[2:3], v[2:3], 0, s[8:9]
	global_load_dword v20, v[2:3], off
	v_lshl_add_u64 v[2:3], v[2:3], 0, s[8:9]
	global_load_dword v21, v[2:3], off
	s_waitcnt vmcnt(0)
	v_mul_f32_e32 v7, 0x3fb8aa3b, v7
	v_mul_f32_e32 v8, 0x3fb8aa3b, v8
	v_mul_f32_e32 v9, 0x3fb8aa3b, v9
	v_mul_f32_e32 v10, 0x3fb8aa3b, v10
	v_mul_f32_e32 v11, 0x3fb8aa3b, v11
	v_mul_f32_e32 v12, 0x3fb8aa3b, v12
	v_mul_f32_e32 v13, 0x3fb8aa3b, v13
	v_mul_f32_e32 v14, 0x3fb8aa3b, v14
	v_mul_f32_e32 v15, 0x3fb8aa3b, v15
	v_mul_f32_e32 v16, 0x3fb8aa3b, v16
	v_mul_f32_e32 v17, 0x3fb8aa3b, v17
	v_mul_f32_e32 v18, 0x3fb8aa3b, v18
	v_mul_f32_e32 v19, 0x3fb8aa3b, v19
	v_mul_f32_e32 v20, 0x3fb8aa3b, v20
	v_mul_f32_e32 v21, 0x3fb8aa3b, v21
	s_mov_b64 exec, s[0:1]
	ds_write_b32 v4, v7
	ds_write_b32 v4, v8 offset:2048
	ds_write_b32 v4, v9 offset:4096
	ds_write_b32 v4, v10 offset:6144
	ds_write_b32 v4, v11 offset:8192
	ds_write_b32 v4, v12 offset:10240
	ds_write_b32 v4, v13 offset:12288
	ds_write_b32 v4, v14 offset:14336
	ds_write_b32 v4, v15 offset:16384
	ds_write_b32 v4, v16 offset:18432
	ds_write_b32 v4, v17 offset:20480
	ds_write_b32 v4, v18 offset:22528
	ds_write_b32 v4, v19 offset:24576
	ds_write_b32 v4, v20 offset:26624
	ds_write_b32 v4, v21 offset:28672
	s_mov_b64 s[6:7], 0
